# in-proj GEMM K-loop: LDS-DMA issues re-balanced 4/4/4/4 over the four load phases (A half-0 pieces staged one phase later, SP2 waits vmcnt(6))
# speedup vs baseline: 1.0056x; 1.0003x over previous
.LBB0_314:
	s_add_u32 s20, s55, s4
	s_addc_u32 s21, s56, s5
	s_add_u32 s22, s20, 0x4500100
	s_addc_u32 s23, s21, 0
	s_add_u32 s24, s57, s4
	s_addc_u32 s25, s58, s5
	s_add_u32 s26, s24, 0x100100
	s_addc_u32 s27, s25, 0
	s_add_u32 s20, s20, 0x4500180
	s_addc_u32 s21, s21, 0
	s_add_u32 s60, s24, 0x100180
	s_addc_u32 s61, s25, 0
	s_cmpk_eq_i32 s4, 0x700
	s_cselect_b32 s25, s17, s23
	s_cselect_b32 s24, s15, s22
	s_cselect_b32 s27, s19, s27
	s_cselect_b32 s26, s13, s26
	s_cselect_b32 s21, s52, s21
	s_cselect_b32 s20, s51, s20
	s_cselect_b32 s23, s54, s61
	s_cselect_b32 s22, s53, s60
	s_add_i32 s60, 0, 0x10000
	v_add_u32_e32 v168, s60, v161
	s_add_i32 s61, 0, 0x14000
	ds_read_b128 v[100:103], v168
	ds_read_b128 v[112:115], v168 offset:1024
	ds_read_b128 v[116:119], v168 offset:2048
	ds_read_b128 v[172:175], v168 offset:3072
	v_add_u32_e32 v168, s61, v161
	ds_read_b128 v[176:179], v168
	ds_read_b128 v[180:183], v168 offset:1024
	ds_read_b128 v[184:187], v168 offset:2048
	ds_read_b128 v[188:191], v168 offset:3072
	v_lshl_add_u64 v[168:169], v[98:99], 0, s[4:5]
	s_add_i32 m0, s39, 0xc000
	ds_read_b128 v[192:195], v170
	ds_read_b128 v[196:199], v170 offset:1024
	ds_read_b128 v[200:203], v170 offset:2048
	ds_read_b128 v[204:207], v170 offset:3072
	ds_read_b128 v[210:213], v170 offset:4096
	ds_read_b128 v[216:219], v170 offset:5120
	ds_read_b128 v[226:229], v170 offset:6144
	ds_read_b128 v[232:235], v170 offset:7168
	global_load_lds_dwordx4 v[168:169], off
	v_lshl_add_u64 v[168:169], v[96:97], 0, s[4:5]
	s_add_i32 m0, s39, 0xe000
	s_nop 0
	global_load_lds_dwordx4 v[168:169], off
	s_waitcnt vmcnt(8)
	s_waitcnt lgkmcnt(0)
	s_barrier
	s_setprio 1
	s_waitcnt lgkmcnt(0)
	v_mfma_f32_16x16x32_bf16 v[140:143], v[100:103], v[192:195], v[140:143]
	v_mfma_f32_16x16x32_bf16 v[136:139], v[116:119], v[192:195], v[136:139]
	v_mfma_f32_16x16x32_bf16 v[124:127], v[100:103], v[200:203], v[124:127]
	v_mfma_f32_16x16x32_bf16 v[120:123], v[116:119], v[200:203], v[120:123]
	v_mfma_f32_16x16x32_bf16 v[92:95], v[100:103], v[210:213], v[92:95]
	v_mfma_f32_16x16x32_bf16 v[88:91], v[116:119], v[210:213], v[88:91]
	v_mfma_f32_16x16x32_bf16 v[76:79], v[100:103], v[226:229], v[76:79]
	v_mfma_f32_16x16x32_bf16 v[72:75], v[116:119], v[226:229], v[72:75]
	v_mfma_f32_16x16x32_bf16 v[140:143], v[112:115], v[196:199], v[140:143]
	v_mfma_f32_16x16x32_bf16 v[136:139], v[172:175], v[196:199], v[136:139]
	v_mfma_f32_16x16x32_bf16 v[124:127], v[112:115], v[204:207], v[124:127]
	v_mfma_f32_16x16x32_bf16 v[120:123], v[172:175], v[204:207], v[120:123]
	v_mfma_f32_16x16x32_bf16 v[92:95], v[112:115], v[216:219], v[92:95]
	v_mfma_f32_16x16x32_bf16 v[88:91], v[172:175], v[216:219], v[88:91]
	v_mfma_f32_16x16x32_bf16 v[76:79], v[112:115], v[232:235], v[76:79]
	v_mfma_f32_16x16x32_bf16 v[72:75], v[172:175], v[232:235], v[72:75]
	s_setprio 0
	s_setprio 1
	v_mfma_f32_16x16x32_bf16 v[132:135], v[176:179], v[192:195], v[132:135]
	v_mfma_f32_16x16x32_bf16 v[128:131], v[184:187], v[192:195], v[128:131]
	v_mfma_f32_16x16x32_bf16 v[108:111], v[176:179], v[200:203], v[108:111]
	v_mfma_f32_16x16x32_bf16 v[104:107], v[184:187], v[200:203], v[104:107]
	v_mfma_f32_16x16x32_bf16 v[84:87], v[176:179], v[210:213], v[84:87]
	v_mfma_f32_16x16x32_bf16 v[80:83], v[184:187], v[210:213], v[80:83]
	v_mfma_f32_16x16x32_bf16 v[68:71], v[176:179], v[226:229], v[68:71]
	v_mfma_f32_16x16x32_bf16 v[64:67], v[184:187], v[226:229], v[64:67]
	v_mfma_f32_16x16x32_bf16 v[132:135], v[180:183], v[196:199], v[132:135]
	v_mfma_f32_16x16x32_bf16 v[128:131], v[188:191], v[196:199], v[128:131]
	v_mfma_f32_16x16x32_bf16 v[108:111], v[180:183], v[204:207], v[108:111]
	v_mfma_f32_16x16x32_bf16 v[104:107], v[188:191], v[204:207], v[104:107]
	v_mfma_f32_16x16x32_bf16 v[84:87], v[180:183], v[216:219], v[84:87]
	v_mfma_f32_16x16x32_bf16 v[80:83], v[188:191], v[216:219], v[80:83]
	v_mfma_f32_16x16x32_bf16 v[68:71], v[180:183], v[232:235], v[68:71]
	v_mfma_f32_16x16x32_bf16 v[64:67], v[188:191], v[232:235], v[64:67]
	s_setprio 0
	s_barrier
	s_add_i32 s60, s60, s38
	v_lshl_add_u64 v[168:169], s[26:27], 0, v[150:151]
	s_mov_b32 m0, s60
	ds_read_b128 v[192:195], v170 offset:16384
	ds_read_b128 v[196:199], v170 offset:17408
	ds_read_b128 v[200:203], v170 offset:18432
	ds_read_b128 v[204:207], v170 offset:19456
	ds_read_b128 v[210:213], v170 offset:20480
	ds_read_b128 v[216:219], v170 offset:21504
	ds_read_b128 v[226:229], v170 offset:22528
	ds_read_b128 v[232:235], v170 offset:23552
	global_load_lds_dwordx4 v[168:169], off
	s_add_i32 m0, s60, 0x2000
	v_lshl_add_u64 v[168:169], s[26:27], 0, v[144:145]
	s_add_u32 s26, s26, 0x10000
	s_addc_u32 s27, s27, 0
	s_add_i32 s60, s61, s38
	global_load_lds_dwordx4 v[168:169], off
	v_lshl_add_u64 v[168:169], s[26:27], 0, v[150:151]
	s_mov_b32 m0, s60
	s_nop 0
	global_load_lds_dwordx4 v[168:169], off
	v_lshl_add_u64 v[168:169], s[26:27], 0, v[144:145]
	s_add_i32 m0, s60, 0x2000
	s_nop 0
	global_load_lds_dwordx4 v[168:169], off
	s_waitcnt vmcnt(6)
	s_waitcnt lgkmcnt(0)
	s_barrier
	s_setprio 1
	s_waitcnt lgkmcnt(0)
	v_mfma_f32_16x16x32_bf16 v[52:55], v[100:103], v[192:195], v[52:55]
	v_mfma_f32_16x16x32_bf16 v[48:51], v[116:119], v[192:195], v[48:51]
	v_mfma_f32_16x16x32_bf16 v[36:39], v[100:103], v[200:203], v[36:39]
	v_mfma_f32_16x16x32_bf16 v[32:35], v[116:119], v[200:203], v[32:35]
	v_mfma_f32_16x16x32_bf16 v[20:23], v[100:103], v[210:213], v[20:23]
	v_mfma_f32_16x16x32_bf16 v[16:19], v[116:119], v[210:213], v[16:19]
	v_mfma_f32_16x16x32_bf16 v[4:7], v[100:103], v[226:229], v[4:7]
	v_mfma_f32_16x16x32_bf16 v[0:3], v[116:119], v[226:229], v[0:3]
	v_mfma_f32_16x16x32_bf16 v[52:55], v[112:115], v[196:199], v[52:55]
	v_mfma_f32_16x16x32_bf16 v[48:51], v[172:175], v[196:199], v[48:51]
	v_mfma_f32_16x16x32_bf16 v[36:39], v[112:115], v[204:207], v[36:39]
	v_mfma_f32_16x16x32_bf16 v[32:35], v[172:175], v[204:207], v[32:35]
	v_mfma_f32_16x16x32_bf16 v[20:23], v[112:115], v[216:219], v[20:23]
	v_mfma_f32_16x16x32_bf16 v[16:19], v[172:175], v[216:219], v[16:19]
	v_mfma_f32_16x16x32_bf16 v[4:7], v[112:115], v[232:235], v[4:7]
	v_mfma_f32_16x16x32_bf16 v[0:3], v[172:175], v[232:235], v[0:3]
	s_setprio 0
	s_setprio 1
	v_mfma_f32_16x16x32_bf16 v[60:63], v[176:179], v[192:195], v[60:63]
	v_mfma_f32_16x16x32_bf16 v[56:59], v[184:187], v[192:195], v[56:59]
	v_mfma_f32_16x16x32_bf16 v[44:47], v[176:179], v[200:203], v[44:47]
	v_mfma_f32_16x16x32_bf16 v[40:43], v[184:187], v[200:203], v[40:43]
	v_mfma_f32_16x16x32_bf16 v[28:31], v[176:179], v[210:213], v[28:31]
	v_mfma_f32_16x16x32_bf16 v[24:27], v[184:187], v[210:213], v[24:27]
	v_mfma_f32_16x16x32_bf16 v[12:15], v[176:179], v[226:229], v[12:15]
	v_mfma_f32_16x16x32_bf16 v[8:11], v[184:187], v[226:229], v[8:11]
	v_mfma_f32_16x16x32_bf16 v[60:63], v[180:183], v[196:199], v[60:63]
	v_mfma_f32_16x16x32_bf16 v[56:59], v[188:191], v[196:199], v[56:59]
	v_mfma_f32_16x16x32_bf16 v[44:47], v[180:183], v[204:207], v[44:47]
	v_mfma_f32_16x16x32_bf16 v[40:43], v[188:191], v[204:207], v[40:43]
	v_mfma_f32_16x16x32_bf16 v[28:31], v[180:183], v[216:219], v[28:31]
	v_mfma_f32_16x16x32_bf16 v[24:27], v[188:191], v[216:219], v[24:27]
	v_mfma_f32_16x16x32_bf16 v[12:15], v[180:183], v[232:235], v[12:15]
	v_mfma_f32_16x16x32_bf16 v[8:11], v[188:191], v[232:235], v[8:11]
	s_setprio 0
	s_barrier
	s_add_i32 s26, 0, 0x18000
	v_add_u32_e32 v168, s26, v161
	s_add_i32 s27, 0, 0x1c000
	ds_read_b128 v[100:103], v168
	ds_read_b128 v[112:115], v168 offset:1024
	ds_read_b128 v[116:119], v168 offset:2048
	ds_read_b128 v[172:175], v168 offset:3072
	v_add_u32_e32 v168, s27, v161
	ds_read_b128 v[176:179], v168
	ds_read_b128 v[180:183], v168 offset:1024
	ds_read_b128 v[184:187], v168 offset:2048
	ds_read_b128 v[188:191], v168 offset:3072
	v_lshl_add_u64 v[168:169], s[24:25], 0, v[152:153]
	s_mov_b32 m0, s39
	s_nop 0
	global_load_lds_dwordx4 v[168:169], off
	v_lshl_add_u64 v[168:169], s[24:25], 0, v[146:147]
	s_mov_b32 m0, s40
	s_nop 0
	global_load_lds_dwordx4 v[168:169], off
	s_mov_b32 m0, s41
	v_lshl_add_u64 v[168:169], s[24:25], 0, v[154:155]
	ds_read_b128 v[192:195], v170 offset:32768
	ds_read_b128 v[196:199], v170 offset:33792
	ds_read_b128 v[200:203], v170 offset:34816
	ds_read_b128 v[204:207], v170 offset:35840
	ds_read_b128 v[210:213], v170 offset:36864
	ds_read_b128 v[216:219], v170 offset:37888
	ds_read_b128 v[226:229], v170 offset:38912
	ds_read_b128 v[232:235], v170 offset:39936
	global_load_lds_dwordx4 v[168:169], off
	v_lshl_add_u64 v[168:169], s[24:25], 0, v[148:149]
	s_mov_b32 m0, s42
	s_nop 0
	global_load_lds_dwordx4 v[168:169], off
	s_waitcnt vmcnt(8)
	s_waitcnt lgkmcnt(0)
	s_barrier
	s_setprio 1
	s_waitcnt lgkmcnt(0)
	v_mfma_f32_16x16x32_bf16 v[140:143], v[100:103], v[192:195], v[140:143]
	v_mfma_f32_16x16x32_bf16 v[136:139], v[116:119], v[192:195], v[136:139]
	v_mfma_f32_16x16x32_bf16 v[124:127], v[100:103], v[200:203], v[124:127]
	v_mfma_f32_16x16x32_bf16 v[120:123], v[116:119], v[200:203], v[120:123]
	v_mfma_f32_16x16x32_bf16 v[92:95], v[100:103], v[210:213], v[92:95]
	v_mfma_f32_16x16x32_bf16 v[88:91], v[116:119], v[210:213], v[88:91]
	v_mfma_f32_16x16x32_bf16 v[76:79], v[100:103], v[226:229], v[76:79]
	v_mfma_f32_16x16x32_bf16 v[72:75], v[116:119], v[226:229], v[72:75]
	v_mfma_f32_16x16x32_bf16 v[140:143], v[112:115], v[196:199], v[140:143]
	v_mfma_f32_16x16x32_bf16 v[136:139], v[172:175], v[196:199], v[136:139]
	v_mfma_f32_16x16x32_bf16 v[124:127], v[112:115], v[204:207], v[124:127]
	v_mfma_f32_16x16x32_bf16 v[120:123], v[172:175], v[204:207], v[120:123]
	v_mfma_f32_16x16x32_bf16 v[92:95], v[112:115], v[216:219], v[92:95]
	v_mfma_f32_16x16x32_bf16 v[88:91], v[172:175], v[216:219], v[88:91]
	v_mfma_f32_16x16x32_bf16 v[76:79], v[112:115], v[232:235], v[76:79]
	v_mfma_f32_16x16x32_bf16 v[72:75], v[172:175], v[232:235], v[72:75]
	s_setprio 0
	s_setprio 1
	v_mfma_f32_16x16x32_bf16 v[132:135], v[176:179], v[192:195], v[132:135]
	v_mfma_f32_16x16x32_bf16 v[128:131], v[184:187], v[192:195], v[128:131]
	v_mfma_f32_16x16x32_bf16 v[108:111], v[176:179], v[200:203], v[108:111]
	v_mfma_f32_16x16x32_bf16 v[104:107], v[184:187], v[200:203], v[104:107]
	v_mfma_f32_16x16x32_bf16 v[84:87], v[176:179], v[210:213], v[84:87]
	v_mfma_f32_16x16x32_bf16 v[80:83], v[184:187], v[210:213], v[80:83]
	v_mfma_f32_16x16x32_bf16 v[68:71], v[176:179], v[226:229], v[68:71]
	v_mfma_f32_16x16x32_bf16 v[64:67], v[184:187], v[226:229], v[64:67]
	v_mfma_f32_16x16x32_bf16 v[132:135], v[180:183], v[196:199], v[132:135]
	v_mfma_f32_16x16x32_bf16 v[128:131], v[188:191], v[196:199], v[128:131]
	v_mfma_f32_16x16x32_bf16 v[108:111], v[180:183], v[204:207], v[108:111]
	v_mfma_f32_16x16x32_bf16 v[104:107], v[188:191], v[204:207], v[104:107]
	v_mfma_f32_16x16x32_bf16 v[84:87], v[180:183], v[216:219], v[84:87]
	v_mfma_f32_16x16x32_bf16 v[80:83], v[188:191], v[216:219], v[80:83]
	v_mfma_f32_16x16x32_bf16 v[68:71], v[180:183], v[232:235], v[68:71]
	v_mfma_f32_16x16x32_bf16 v[64:67], v[188:191], v[232:235], v[64:67]
	s_setprio 0
	s_barrier
	s_add_i32 s24, s26, s38
	v_lshl_add_u64 v[168:169], s[22:23], 0, v[150:151]
	s_mov_b32 m0, s24
	ds_read_b128 v[192:195], v170 offset:49152
	ds_read_b128 v[196:199], v170 offset:50176
	ds_read_b128 v[200:203], v170 offset:51200
	ds_read_b128 v[204:207], v170 offset:52224
	ds_read_b128 v[210:213], v170 offset:53248
	ds_read_b128 v[216:219], v170 offset:54272
	ds_read_b128 v[226:229], v170 offset:55296
	ds_read_b128 v[232:235], v170 offset:56320
	global_load_lds_dwordx4 v[168:169], off
	s_add_i32 m0, s24, 0x2000
	v_lshl_add_u64 v[168:169], s[22:23], 0, v[144:145]
	s_add_u32 s22, s22, 0x10000
	s_addc_u32 s23, s23, 0
	s_add_i32 s24, s27, s38
	global_load_lds_dwordx4 v[168:169], off
	v_lshl_add_u64 v[168:169], s[22:23], 0, v[150:151]
	s_mov_b32 m0, s24
	s_nop 0
	global_load_lds_dwordx4 v[168:169], off
	v_lshl_add_u64 v[168:169], s[22:23], 0, v[144:145]
	s_add_i32 m0, s24, 0x2000
	s_nop 0
	global_load_lds_dwordx4 v[168:169], off
	s_waitcnt vmcnt(6)
	s_waitcnt lgkmcnt(0)
	s_barrier
	s_setprio 1
	s_waitcnt lgkmcnt(0)
	v_mfma_f32_16x16x32_bf16 v[52:55], v[100:103], v[192:195], v[52:55]
	v_mfma_f32_16x16x32_bf16 v[48:51], v[116:119], v[192:195], v[48:51]
	v_mfma_f32_16x16x32_bf16 v[36:39], v[100:103], v[200:203], v[36:39]
	v_mfma_f32_16x16x32_bf16 v[32:35], v[116:119], v[200:203], v[32:35]
	v_mfma_f32_16x16x32_bf16 v[20:23], v[100:103], v[210:213], v[20:23]
	v_mfma_f32_16x16x32_bf16 v[16:19], v[116:119], v[210:213], v[16:19]
	v_mfma_f32_16x16x32_bf16 v[4:7], v[100:103], v[226:229], v[4:7]
	v_mfma_f32_16x16x32_bf16 v[0:3], v[116:119], v[226:229], v[0:3]
	v_mfma_f32_16x16x32_bf16 v[52:55], v[112:115], v[196:199], v[52:55]
	v_mfma_f32_16x16x32_bf16 v[48:51], v[172:175], v[196:199], v[48:51]
	v_mfma_f32_16x16x32_bf16 v[36:39], v[112:115], v[204:207], v[36:39]
	v_mfma_f32_16x16x32_bf16 v[32:35], v[172:175], v[204:207], v[32:35]
	v_mfma_f32_16x16x32_bf16 v[20:23], v[112:115], v[216:219], v[20:23]
	v_mfma_f32_16x16x32_bf16 v[16:19], v[172:175], v[216:219], v[16:19]
	v_mfma_f32_16x16x32_bf16 v[4:7], v[112:115], v[232:235], v[4:7]
	v_mfma_f32_16x16x32_bf16 v[0:3], v[172:175], v[232:235], v[0:3]
	s_setprio 0
	s_setprio 1
	v_mfma_f32_16x16x32_bf16 v[60:63], v[176:179], v[192:195], v[60:63]
	v_mfma_f32_16x16x32_bf16 v[56:59], v[184:187], v[192:195], v[56:59]
	v_mfma_f32_16x16x32_bf16 v[44:47], v[176:179], v[200:203], v[44:47]
	v_mfma_f32_16x16x32_bf16 v[40:43], v[184:187], v[200:203], v[40:43]
	v_mfma_f32_16x16x32_bf16 v[28:31], v[176:179], v[210:213], v[28:31]
	v_mfma_f32_16x16x32_bf16 v[24:27], v[184:187], v[210:213], v[24:27]
	v_mfma_f32_16x16x32_bf16 v[12:15], v[176:179], v[226:229], v[12:15]
	v_mfma_f32_16x16x32_bf16 v[8:11], v[184:187], v[226:229], v[8:11]
	v_mfma_f32_16x16x32_bf16 v[60:63], v[180:183], v[196:199], v[60:63]
	v_mfma_f32_16x16x32_bf16 v[56:59], v[188:191], v[196:199], v[56:59]
	v_mfma_f32_16x16x32_bf16 v[44:47], v[180:183], v[204:207], v[44:47]
	v_mfma_f32_16x16x32_bf16 v[40:43], v[188:191], v[204:207], v[40:43]
	v_mfma_f32_16x16x32_bf16 v[28:31], v[180:183], v[216:219], v[28:31]
	v_mfma_f32_16x16x32_bf16 v[24:27], v[188:191], v[216:219], v[24:27]
	v_mfma_f32_16x16x32_bf16 v[12:15], v[180:183], v[232:235], v[12:15]
	v_mfma_f32_16x16x32_bf16 v[8:11], v[188:191], v[232:235], v[8:11]
	s_setprio 0
	s_barrier
	v_lshl_add_u64 v[168:169], s[20:21], 0, v[152:153]
	s_mov_b32 m0, s47
	s_nop 0
	global_load_lds_dwordx4 v[168:169], off
	v_lshl_add_u64 v[168:169], s[20:21], 0, v[146:147]
	s_mov_b32 m0, s48
	s_nop 0
	global_load_lds_dwordx4 v[168:169], off
	s_add_i32 s59, s59, 2
	s_add_u32 s4, s4, 0x100
	s_addc_u32 s5, s5, 0
	s_cmp_gt_u32 s59, 13
	s_cbranch_scc0 .LBB0_314
	s_and_b64 vcc, exec, s[10:11]
	s_cbranch_vccz .LBB0_317
	s_barrier
